# recfin fin-epilogue bias loads issued at start of fin phase (on top of v67)
# baseline (speedup 1.0000x reference)
.LBB6_72:
	s_or_b64 exec, exec, s[2:3]
	s_waitcnt vmcnt(18)
	v_lshrrev_b32_e32 v70, 6, v0
	v_lshrrev_b32_e32 v71, 5, v182
	s_waitcnt lgkmcnt(0)
	s_barrier
	ds_read_b128 v[66:69], v183 offset:4896
	ds_read_b128 v[86:89], v183
	s_waitcnt vmcnt(17) lgkmcnt(0)
	v_mfma_f32_32x32x16_f16 v[50:65], v[158:161], v[86:89], v[50:65]
	ds_read_b128 v[86:89], v183 offset:9792
	v_mfma_f32_32x32x16_f16 v[34:49], v[158:161], v[66:69], v[34:49]
	ds_read_b128 v[66:69], v183 offset:14688
	s_waitcnt lgkmcnt(1)
	v_mfma_f32_32x32x16_f16 v[18:33], v[158:161], v[86:89], v[18:33]
	ds_read_b128 v[86:89], v183 offset:64
	s_waitcnt lgkmcnt(1)
	v_mfma_f32_32x32x16_f16 v[2:17], v[158:161], v[66:69], v[2:17]
	ds_read_b128 v[66:69], v183 offset:4960
	s_waitcnt vmcnt(16) lgkmcnt(1)
	v_mfma_f32_32x32x16_f16 v[50:65], v[154:157], v[86:89], v[50:65]
	ds_read_b128 v[86:89], v183 offset:9856
	s_waitcnt lgkmcnt(1)
	v_mfma_f32_32x32x16_f16 v[34:49], v[154:157], v[66:69], v[34:49]
	ds_read_b128 v[66:69], v183 offset:14752
	s_waitcnt lgkmcnt(1)
	v_mfma_f32_32x32x16_f16 v[18:33], v[154:157], v[86:89], v[18:33]
	ds_read_b128 v[86:89], v183 offset:144
	s_waitcnt lgkmcnt(1)
	v_mfma_f32_32x32x16_f16 v[2:17], v[154:157], v[66:69], v[2:17]
	ds_read_b128 v[66:69], v183 offset:5040
	s_waitcnt vmcnt(15) lgkmcnt(1)
	v_mfma_f32_32x32x16_f16 v[50:65], v[146:149], v[86:89], v[50:65]
	ds_read_b128 v[86:89], v183 offset:9936
	s_waitcnt lgkmcnt(1)
	v_mfma_f32_32x32x16_f16 v[34:49], v[146:149], v[66:69], v[34:49]
	ds_read_b128 v[66:69], v183 offset:14832
	s_waitcnt lgkmcnt(1)
	v_mfma_f32_32x32x16_f16 v[18:33], v[146:149], v[86:89], v[18:33]
	ds_read_b128 v[86:89], v183 offset:208
	s_waitcnt lgkmcnt(1)
	v_mfma_f32_32x32x16_f16 v[2:17], v[146:149], v[66:69], v[2:17]
	ds_read_b128 v[66:69], v183 offset:5104
	s_waitcnt vmcnt(14) lgkmcnt(1)
	v_mfma_f32_32x32x16_f16 v[50:65], v[142:145], v[86:89], v[50:65]
	ds_read_b128 v[86:89], v183 offset:10000
	s_waitcnt lgkmcnt(1)
	v_mfma_f32_32x32x16_f16 v[34:49], v[142:145], v[66:69], v[34:49]
	ds_read_b128 v[66:69], v183 offset:14896
	s_waitcnt lgkmcnt(1)
	v_mfma_f32_32x32x16_f16 v[18:33], v[142:145], v[86:89], v[18:33]
	ds_read_b128 v[86:89], v183 offset:288
	s_waitcnt lgkmcnt(1)
	v_mfma_f32_32x32x16_f16 v[2:17], v[142:145], v[66:69], v[2:17]
	ds_read_b128 v[66:69], v183 offset:5184
	s_waitcnt vmcnt(13) lgkmcnt(1)
	v_mfma_f32_32x32x16_f16 v[50:65], v[134:137], v[86:89], v[50:65]
	ds_read_b128 v[86:89], v183 offset:10080
	s_waitcnt lgkmcnt(1)
	v_mfma_f32_32x32x16_f16 v[34:49], v[134:137], v[66:69], v[34:49]
	ds_read_b128 v[66:69], v183 offset:14976
	s_waitcnt lgkmcnt(1)
	v_mfma_f32_32x32x16_f16 v[18:33], v[134:137], v[86:89], v[18:33]
	ds_read_b128 v[86:89], v183 offset:352
	s_waitcnt lgkmcnt(1)
	v_mfma_f32_32x32x16_f16 v[2:17], v[134:137], v[66:69], v[2:17]
	ds_read_b128 v[66:69], v183 offset:5248
	s_waitcnt vmcnt(12) lgkmcnt(1)
	v_mfma_f32_32x32x16_f16 v[50:65], v[130:133], v[86:89], v[50:65]
	ds_read_b128 v[86:89], v183 offset:10144
	s_waitcnt lgkmcnt(1)
	v_mfma_f32_32x32x16_f16 v[34:49], v[130:133], v[66:69], v[34:49]
	ds_read_b128 v[66:69], v183 offset:15040
	s_waitcnt lgkmcnt(1)
	v_mfma_f32_32x32x16_f16 v[18:33], v[130:133], v[86:89], v[18:33]
	ds_read_b128 v[86:89], v183 offset:4896
	s_waitcnt lgkmcnt(1)
	v_mfma_f32_32x32x16_f16 v[2:17], v[130:133], v[66:69], v[2:17]
	ds_read_b128 v[66:69], v183 offset:9792
	s_waitcnt vmcnt(11) lgkmcnt(1)
	v_mfma_f32_32x32x16_f16 v[50:65], v[126:129], v[86:89], v[50:65]
	ds_read_b128 v[86:89], v183 offset:14688
	s_waitcnt lgkmcnt(1)
	v_mfma_f32_32x32x16_f16 v[34:49], v[126:129], v[66:69], v[34:49]
	ds_read_b128 v[66:69], v183 offset:19584
	s_waitcnt lgkmcnt(1)
	v_mfma_f32_32x32x16_f16 v[18:33], v[126:129], v[86:89], v[18:33]
	ds_read_b128 v[86:89], v183 offset:4960
	s_waitcnt lgkmcnt(1)
	v_mfma_f32_32x32x16_f16 v[2:17], v[126:129], v[66:69], v[2:17]
	ds_read_b128 v[66:69], v183 offset:9856
	s_waitcnt vmcnt(10) lgkmcnt(1)
	v_mfma_f32_32x32x16_f16 v[50:65], v[122:125], v[86:89], v[50:65]
	ds_read_b128 v[86:89], v183 offset:14752
	s_waitcnt lgkmcnt(1)
	v_mfma_f32_32x32x16_f16 v[34:49], v[122:125], v[66:69], v[34:49]
	ds_read_b128 v[66:69], v183 offset:19648
	s_waitcnt lgkmcnt(1)
	v_mfma_f32_32x32x16_f16 v[18:33], v[122:125], v[86:89], v[18:33]
	ds_read_b128 v[86:89], v183 offset:5040
	s_waitcnt lgkmcnt(1)
	v_mfma_f32_32x32x16_f16 v[2:17], v[122:125], v[66:69], v[2:17]
	ds_read_b128 v[66:69], v183 offset:9936
	s_waitcnt vmcnt(9) lgkmcnt(1)
	v_mfma_f32_32x32x16_f16 v[50:65], v[118:121], v[86:89], v[50:65]
	ds_read_b128 v[86:89], v183 offset:14832
	s_waitcnt lgkmcnt(1)
	v_mfma_f32_32x32x16_f16 v[34:49], v[118:121], v[66:69], v[34:49]
	ds_read_b128 v[66:69], v183 offset:19728
	s_waitcnt lgkmcnt(1)
	v_mfma_f32_32x32x16_f16 v[18:33], v[118:121], v[86:89], v[18:33]
	ds_read_b128 v[86:89], v183 offset:5104
	s_waitcnt lgkmcnt(1)
	v_mfma_f32_32x32x16_f16 v[2:17], v[118:121], v[66:69], v[2:17]
	ds_read_b128 v[66:69], v183 offset:10000
	s_waitcnt vmcnt(8) lgkmcnt(1)
	v_mfma_f32_32x32x16_f16 v[50:65], v[114:117], v[86:89], v[50:65]
	ds_read_b128 v[86:89], v183 offset:14896
	s_waitcnt lgkmcnt(1)
	v_mfma_f32_32x32x16_f16 v[34:49], v[114:117], v[66:69], v[34:49]
	ds_read_b128 v[66:69], v183 offset:19792
	s_waitcnt lgkmcnt(1)
	v_mfma_f32_32x32x16_f16 v[18:33], v[114:117], v[86:89], v[18:33]
	ds_read_b128 v[86:89], v183 offset:5184
	s_waitcnt lgkmcnt(1)
	v_mfma_f32_32x32x16_f16 v[2:17], v[114:117], v[66:69], v[2:17]
	ds_read_b128 v[66:69], v183 offset:10080
	s_waitcnt vmcnt(7) lgkmcnt(1)
	v_mfma_f32_32x32x16_f16 v[50:65], v[110:113], v[86:89], v[50:65]
	ds_read_b128 v[86:89], v183 offset:14976
	s_waitcnt lgkmcnt(1)
	v_mfma_f32_32x32x16_f16 v[34:49], v[110:113], v[66:69], v[34:49]
	ds_read_b128 v[66:69], v183 offset:19872
	s_waitcnt lgkmcnt(1)
	v_mfma_f32_32x32x16_f16 v[18:33], v[110:113], v[86:89], v[18:33]
	ds_read_b128 v[86:89], v183 offset:5248
	s_waitcnt lgkmcnt(1)
	v_mfma_f32_32x32x16_f16 v[2:17], v[110:113], v[66:69], v[2:17]
	ds_read_b128 v[66:69], v183 offset:10144
	s_waitcnt vmcnt(6) lgkmcnt(1)
	v_mfma_f32_32x32x16_f16 v[50:65], v[106:109], v[86:89], v[50:65]
	ds_read_b128 v[86:89], v183 offset:15040
	s_waitcnt lgkmcnt(1)
	v_mfma_f32_32x32x16_f16 v[34:49], v[106:109], v[66:69], v[34:49]
	ds_read_b128 v[66:69], v183 offset:19936
	s_waitcnt lgkmcnt(1)
	v_mfma_f32_32x32x16_f16 v[18:33], v[106:109], v[86:89], v[18:33]
	ds_read_b128 v[86:89], v183 offset:9792
	s_waitcnt lgkmcnt(1)
	v_mfma_f32_32x32x16_f16 v[2:17], v[106:109], v[66:69], v[2:17]
	ds_read_b128 v[66:69], v183 offset:14688
	s_waitcnt vmcnt(5) lgkmcnt(1)
	v_mfma_f32_32x32x16_f16 v[50:65], v[102:105], v[86:89], v[50:65]
	ds_read_b128 v[86:89], v183 offset:19584
	s_waitcnt lgkmcnt(1)
	v_mfma_f32_32x32x16_f16 v[34:49], v[102:105], v[66:69], v[34:49]
	ds_read_b128 v[66:69], v183 offset:24480
	s_waitcnt lgkmcnt(1)
	v_mfma_f32_32x32x16_f16 v[18:33], v[102:105], v[86:89], v[18:33]
	ds_read_b128 v[86:89], v183 offset:9856
	s_waitcnt lgkmcnt(1)
	v_mfma_f32_32x32x16_f16 v[2:17], v[102:105], v[66:69], v[2:17]
	ds_read_b128 v[66:69], v183 offset:14752
	s_waitcnt vmcnt(4) lgkmcnt(1)
	v_mfma_f32_32x32x16_f16 v[50:65], v[94:97], v[86:89], v[50:65]
	ds_read_b128 v[86:89], v183 offset:19648
	s_waitcnt lgkmcnt(1)
	v_mfma_f32_32x32x16_f16 v[34:49], v[94:97], v[66:69], v[34:49]
	ds_read_b128 v[66:69], v183 offset:24544
	s_waitcnt lgkmcnt(1)
	v_mfma_f32_32x32x16_f16 v[18:33], v[94:97], v[86:89], v[18:33]
	ds_read_b128 v[86:89], v183 offset:9936
	s_waitcnt lgkmcnt(1)
	v_mfma_f32_32x32x16_f16 v[2:17], v[94:97], v[66:69], v[2:17]
	ds_read_b128 v[66:69], v183 offset:14832
	s_waitcnt vmcnt(3) lgkmcnt(1)
	v_mfma_f32_32x32x16_f16 v[50:65], v[90:93], v[86:89], v[50:65]
	ds_read_b128 v[86:89], v183 offset:19728
	s_waitcnt lgkmcnt(1)
	v_mfma_f32_32x32x16_f16 v[34:49], v[90:93], v[66:69], v[34:49]
	ds_read_b128 v[66:69], v183 offset:24624
	s_waitcnt lgkmcnt(1)
	v_mfma_f32_32x32x16_f16 v[18:33], v[90:93], v[86:89], v[18:33]
	ds_read_b128 v[86:89], v183 offset:10000
	s_waitcnt lgkmcnt(1)
	v_mfma_f32_32x32x16_f16 v[2:17], v[90:93], v[66:69], v[2:17]
	ds_read_b128 v[66:69], v183 offset:14896
	s_waitcnt vmcnt(2) lgkmcnt(1)
	v_mfma_f32_32x32x16_f16 v[50:65], v[82:85], v[86:89], v[50:65]
	ds_read_b128 v[86:89], v183 offset:19792
	s_waitcnt lgkmcnt(1)
	v_mfma_f32_32x32x16_f16 v[34:49], v[82:85], v[66:69], v[34:49]
	ds_read_b128 v[66:69], v183 offset:24688
	s_waitcnt lgkmcnt(1)
	v_mfma_f32_32x32x16_f16 v[18:33], v[82:85], v[86:89], v[18:33]
	ds_read_b128 v[86:89], v183 offset:10080
	s_waitcnt lgkmcnt(1)
	v_mfma_f32_32x32x16_f16 v[2:17], v[82:85], v[66:69], v[2:17]
	ds_read_b128 v[66:69], v183 offset:14976
	s_waitcnt vmcnt(1) lgkmcnt(1)
	v_mfma_f32_32x32x16_f16 v[50:65], v[78:81], v[86:89], v[50:65]
	ds_read_b128 v[82:85], v183 offset:19872
	s_waitcnt lgkmcnt(1)
	v_mfma_f32_32x32x16_f16 v[34:49], v[78:81], v[66:69], v[34:49]
	ds_read_b128 v[66:69], v183 offset:24768
	s_waitcnt lgkmcnt(1)
	v_mfma_f32_32x32x16_f16 v[18:33], v[78:81], v[82:85], v[18:33]
	ds_read_b128 v[82:85], v183 offset:10144
	s_waitcnt lgkmcnt(1)
	v_mfma_f32_32x32x16_f16 v[2:17], v[78:81], v[66:69], v[2:17]
	ds_read_b128 v[66:69], v183 offset:15040
	s_waitcnt vmcnt(0) lgkmcnt(1)
	v_mfma_f32_32x32x16_f16 v[50:65], v[74:77], v[82:85], v[50:65]
	ds_read_b128 v[78:81], v183 offset:19936
	s_waitcnt lgkmcnt(1)
	v_mfma_f32_32x32x16_f16 v[34:49], v[74:77], v[66:69], v[34:49]
	ds_read_b128 v[66:69], v183 offset:24832
	s_waitcnt lgkmcnt(1)
	v_mfma_f32_32x32x16_f16 v[18:33], v[74:77], v[78:81], v[18:33]
	s_waitcnt lgkmcnt(0)
	v_mfma_f32_32x32x16_f16 v[2:17], v[74:77], v[66:69], v[2:17]
	v_lshlrev_b32_e32 v66, 2, v71
	v_lshl_or_b32 v74, v70, 5, v66
	v_lshlrev_b32_e32 v80, 2, v74
	s_barrier
	global_load_dwordx4 v[76:79], v80, s[16:17]
	v_lshlrev_b32_e32 v66, 7, v70
	s_movk_i32 s3, 0x210
	v_lshl_or_b32 v66, v71, 3, v66
	v_mad_u32_u24 v73, v180, s3, v66
	global_load_dwordx4 v[66:69], v80, s[16:17] offset:32
	s_mov_b32 s2, 0x41800000
	v_add_u32_e32 v72, 0x4000, v73
	v_add_u32_e32 v71, 0x8000, v73
	s_waitcnt vmcnt(1)
	v_fmamk_f32 v50, v50, 0x3a800000, v76
	v_fmamk_f32 v51, v51, 0x3a800000, v77
	v_fmamk_f32 v52, v52, 0x3a800000, v78
	v_fmamk_f32 v53, v53, 0x3a800000, v79
	v_fmamk_f32 v34, v34, 0x3a800000, v76
	v_fmamk_f32 v35, v35, 0x3a800000, v77
	v_fmamk_f32 v36, v36, 0x3a800000, v78
	v_fmamk_f32 v37, v37, 0x3a800000, v79
	v_fmamk_f32 v18, v18, 0x3a800000, v76
	v_fmamk_f32 v19, v19, 0x3a800000, v77
	v_fmamk_f32 v20, v20, 0x3a800000, v78
	v_fmamk_f32 v21, v21, 0x3a800000, v79
	v_fmamk_f32 v75, v2, 0x3a800000, v76
	v_fmamk_f32 v76, v3, 0x3a800000, v77
	v_fmamk_f32 v77, v4, 0x3a800000, v78
	v_fmac_f32_e32 v79, 0x3a800000, v5
	v_max_f32_e32 v78, 0, v50
	v_max_f32_e32 v81, 0, v51
	v_max_f32_e32 v2, 0, v52
	v_max_f32_e32 v3, 0, v53
	v_max_f32_e32 v82, 0, v34
	v_max_f32_e32 v88, 0, v35
	v_max_f32_e32 v4, 0, v36
	v_max_f32_e32 v5, 0, v37
	v_max_f32_e32 v84, 0, v18
	v_max_f32_e32 v92, 0, v19
	v_max_f32_e32 v18, 0, v20
	v_max_f32_e32 v19, 0, v21
	v_max_f32_e32 v93, 0, v76
	v_max_f32_e32 v20, 0, v77
	v_max_f32_e32 v21, 0, v79
	v_mul_f32_e32 v77, 0x41800000, v78
	v_fma_mixlo_f16 v76, v78, s2, 0
	v_mul_f32_e32 v79, 0x41800000, v81
	v_pk_mul_f32 v[34:35], v[2:3], s[2:3] op_sel_hi:[1,0]
	v_fma_mixlo_f16 v86, v81, s2, 0
	v_mul_f32_e32 v83, 0x41800000, v82
	v_fma_mixlo_f16 v85, v82, s2, 0
	v_mul_f32_e32 v87, 0x41800000, v88
	v_pk_mul_f32 v[36:37], v[4:5], s[2:3] op_sel_hi:[1,0]
	v_fma_mixlo_f16 v76, v78, s2, -v76 op_sel_hi:[0,0,1]
	v_cvt_pk_f16_f32 v78, v77, v79
	v_cvt_pk_f16_f32 v79, v34, v35
	v_fma_mixlo_f16 v89, v88, s2, 0
	v_fma_mixlo_f16 v34, v82, s2, -v85 op_sel_hi:[0,0,1]
	v_cvt_pk_f16_f32 v82, v83, v87
	v_cvt_pk_f16_f32 v83, v36, v37
	v_fma_mixhi_f16 v76, v81, s2, -v86 op_sel_hi:[0,0,1]
	v_cvt_f32_f16_e32 v86, v79
	v_cvt_f32_f16_sdwa v87, v79 dst_sel:DWORD dst_unused:UNUSED_PAD src0_sel:WORD_1
	v_fma_mixhi_f16 v34, v88, s2, -v89 op_sel_hi:[0,0,1]
	v_cvt_f32_f16_e32 v88, v83
	v_cvt_f32_f16_sdwa v89, v83 dst_sel:DWORD dst_unused:UNUSED_PAD src0_sel:WORD_1
	v_pk_mul_f32 v[50:51], v[18:19], s[2:3] op_sel_hi:[1,0]
	v_mul_f32_e32 v90, 0x41800000, v84
	v_fma_mixlo_f16 v91, v84, s2, 0
	v_mul_f32_e32 v94, 0x41800000, v92
	v_pk_mul_f32 v[52:53], v[20:21], s[2:3] op_sel_hi:[1,0]
	v_cvt_pk_f16_f32 v85, v50, v51
	v_pk_fma_f32 v[2:3], v[2:3], s[2:3], v[86:87] op_sel_hi:[1,0,1] neg_lo:[0,0,1] neg_hi:[0,0,1]
	v_fma_mixlo_f16 v36, v84, s2, -v91 op_sel_hi:[0,0,1]
	v_cvt_pk_f16_f32 v84, v90, v94
	v_cvt_f32_f16_e32 v90, v85
	v_cvt_f32_f16_sdwa v91, v85 dst_sel:DWORD dst_unused:UNUSED_PAD src0_sel:WORD_1
	v_pk_fma_f32 v[4:5], v[4:5], s[2:3], v[88:89] op_sel_hi:[1,0,1] neg_lo:[0,0,1] neg_hi:[0,0,1]
	v_cvt_pk_f16_f32 v77, v2, v3
	v_cvt_pk_f16_f32 v3, v52, v53
	v_cvt_pk_f16_f32 v35, v4, v5
	v_cvt_f32_f16_e32 v4, v3
	v_cvt_f32_f16_sdwa v5, v3 dst_sel:DWORD dst_unused:UNUSED_PAD src0_sel:WORD_1
	v_max_f32_e32 v75, 0, v75
	v_fma_mixlo_f16 v97, v75, s2, 0
	v_pk_fma_f32 v[18:19], v[18:19], s[2:3], v[90:91] op_sel_hi:[1,0,1] neg_lo:[0,0,1] neg_hi:[0,0,1]
	v_mul_f32_e32 v96, 0x41800000, v75
	v_mul_f32_e32 v98, 0x41800000, v93
	v_fma_mixlo_f16 v50, v75, s2, -v97 op_sel_hi:[0,0,1]
	v_cvt_pk_f16_f32 v37, v18, v19
	v_fma_mixlo_f16 v18, v93, s2, 0
	v_pk_fma_f32 v[4:5], v[20:21], s[2:3], v[4:5] op_sel_hi:[1,0,1] neg_lo:[0,0,1] neg_hi:[0,0,1]
	v_fma_mixlo_f16 v95, v92, s2, 0
	v_cvt_pk_f16_f32 v2, v96, v98
	v_fma_mixhi_f16 v50, v93, s2, -v18 op_sel_hi:[0,0,1]
	v_cvt_pk_f16_f32 v51, v4, v5
	v_add_u32_e32 v18, 0xc000, v73
	v_fma_mixhi_f16 v36, v92, s2, -v95 op_sel_hi:[0,0,1]
	ds_write2_b64 v73, v[78:79], v[76:77] offset1:2
	ds_write2_b64 v72, v[82:83], v[34:35] offset0:64 offset1:66
	ds_write2_b64 v71, v[84:85], v[36:37] offset0:128 offset1:130
	ds_write2_b64 v18, v[2:3], v[50:51] offset0:192 offset1:194
	s_waitcnt vmcnt(0)
	v_fmamk_f32 v2, v54, 0x3a800000, v66
	v_max_f32_e32 v2, 0, v2
	v_fma_mixlo_f16 v3, v2, s2, 0
	v_mul_f32_e32 v19, 0x41800000, v2
	v_fma_mixlo_f16 v20, v2, s2, -v3 op_sel_hi:[0,0,1]
	v_fmamk_f32 v2, v55, 0x3a800000, v67
	v_max_f32_e32 v21, 0, v2
	v_fmamk_f32 v2, v56, 0x3a800000, v68
	v_fmamk_f32 v35, v57, 0x3a800000, v69
	v_max_f32_e32 v34, 0, v2
	v_max_f32_e32 v35, 0, v35
	v_pk_mul_f32 v[36:37], v[34:35], s[2:3] op_sel_hi:[1,0]
	global_load_dwordx4 v[2:5], v80, s[16:17] offset:64
	v_cvt_pk_f16_f32 v37, v36, v37
	v_cvt_f32_f16_e32 v50, v37
	v_cvt_f32_f16_sdwa v51, v37 dst_sel:DWORD dst_unused:UNUSED_PAD src0_sel:WORD_1
	v_fma_mixlo_f16 v53, v21, s2, 0
	v_mul_f32_e32 v52, 0x41800000, v21
	v_fma_mixhi_f16 v20, v21, s2, -v53 op_sel_hi:[0,0,1]
	v_pk_fma_f32 v[34:35], v[34:35], s[2:3], v[50:51] op_sel_hi:[1,0,1] neg_lo:[0,0,1] neg_hi:[0,0,1]
	v_cvt_pk_f16_f32 v36, v19, v52
	v_cvt_pk_f16_f32 v21, v34, v35
	v_fmamk_f32 v34, v40, 0x3a800000, v68
	v_fmamk_f32 v35, v41, 0x3a800000, v69
	v_fmamk_f32 v19, v38, 0x3a800000, v66
	v_max_f32_e32 v34, 0, v34
	v_max_f32_e32 v35, 0, v35
	ds_write2_b64 v73, v[36:37], v[20:21] offset0:4 offset1:6
	v_max_f32_e32 v19, 0, v19
	v_pk_mul_f32 v[36:37], v[34:35], s[2:3] op_sel_hi:[1,0]
	v_fma_mixlo_f16 v20, v19, s2, 0
	v_cvt_pk_f16_f32 v37, v36, v37
	v_mul_f32_e32 v21, 0x41800000, v19
	v_fma_mixlo_f16 v20, v19, s2, -v20 op_sel_hi:[0,0,1]
	v_fmamk_f32 v19, v39, 0x3a800000, v67
	v_cvt_f32_f16_e32 v38, v37
	v_cvt_f32_f16_sdwa v39, v37 dst_sel:DWORD dst_unused:UNUSED_PAD src0_sel:WORD_1
	v_max_f32_e32 v19, 0, v19
	v_fma_mixlo_f16 v40, v19, s2, 0
	v_mul_f32_e32 v50, 0x41800000, v19
	v_fma_mixhi_f16 v20, v19, s2, -v40 op_sel_hi:[0,0,1]
	v_pk_fma_f32 v[34:35], v[34:35], s[2:3], v[38:39] op_sel_hi:[1,0,1] neg_lo:[0,0,1] neg_hi:[0,0,1]
	v_fmamk_f32 v19, v22, 0x3a800000, v66
	v_cvt_pk_f16_f32 v36, v21, v50
	v_cvt_pk_f16_f32 v21, v34, v35
	v_max_f32_e32 v19, 0, v19
	ds_write2_b64 v72, v[36:37], v[20:21] offset0:68 offset1:70
	v_fma_mixlo_f16 v20, v19, s2, 0
	v_mul_f32_e32 v21, 0x41800000, v19
	v_fma_mixlo_f16 v20, v19, s2, -v20 op_sel_hi:[0,0,1]
	v_fmamk_f32 v19, v23, 0x3a800000, v67
	v_fmamk_f32 v22, v24, 0x3a800000, v68
	v_fmamk_f32 v23, v25, 0x3a800000, v69
	v_max_f32_e32 v22, 0, v22
	v_max_f32_e32 v23, 0, v23
	v_pk_mul_f32 v[24:25], v[22:23], s[2:3] op_sel_hi:[1,0]
	v_max_f32_e32 v19, 0, v19
	v_cvt_pk_f16_f32 v25, v24, v25
	v_cvt_f32_f16_e32 v34, v25
	v_cvt_f32_f16_sdwa v35, v25 dst_sel:DWORD dst_unused:UNUSED_PAD src0_sel:WORD_1
	v_mul_f32_e32 v36, 0x41800000, v19
	v_fma_mixlo_f16 v37, v19, s2, 0
	v_fmamk_f32 v6, v6, 0x3a800000, v66
	v_pk_fma_f32 v[22:23], v[22:23], s[2:3], v[34:35] op_sel_hi:[1,0,1] neg_lo:[0,0,1] neg_hi:[0,0,1]
	v_cvt_pk_f16_f32 v24, v21, v36
	v_fma_mixhi_f16 v20, v19, s2, -v37 op_sel_hi:[0,0,1]
	v_cvt_pk_f16_f32 v21, v22, v23
	v_max_f32_e32 v6, 0, v6
	v_fmamk_f32 v8, v8, 0x3a800000, v68
	v_fmac_f32_e32 v69, 0x3a800000, v9
	ds_write2_b64 v71, v[24:25], v[20:21] offset0:132 offset1:134
	v_fma_mixlo_f16 v20, v6, s2, 0
	v_max_f32_e32 v8, 0, v8
	v_max_f32_e32 v9, 0, v69
	v_mul_f32_e32 v19, 0x41800000, v6
	v_fma_mixlo_f16 v6, v6, s2, -v20 op_sel_hi:[0,0,1]
	v_pk_mul_f32 v[20:21], v[8:9], s[2:3] op_sel_hi:[1,0]
	v_fmamk_f32 v7, v7, 0x3a800000, v67
	v_cvt_pk_f16_f32 v21, v20, v21
	v_cvt_f32_f16_e32 v22, v21
	v_cvt_f32_f16_sdwa v23, v21 dst_sel:DWORD dst_unused:UNUSED_PAD src0_sel:WORD_1
	v_max_f32_e32 v7, 0, v7
	v_mul_f32_e32 v24, 0x41800000, v7
	v_fma_mixlo_f16 v25, v7, s2, 0
	v_pk_fma_f32 v[8:9], v[8:9], s[2:3], v[22:23] op_sel_hi:[1,0,1] neg_lo:[0,0,1] neg_hi:[0,0,1]
	v_cvt_pk_f16_f32 v20, v19, v24
	v_fma_mixhi_f16 v6, v7, s2, -v25 op_sel_hi:[0,0,1]
	v_cvt_pk_f16_f32 v7, v8, v9
	ds_write2_b64 v18, v[20:21], v[6:7] offset0:196 offset1:198
	global_load_dwordx4 v[6:9], v80, s[16:17] offset:96
	s_waitcnt vmcnt(1)
	v_fmamk_f32 v22, v60, 0x3a800000, v4
	v_fmamk_f32 v23, v61, 0x3a800000, v5
	v_max_f32_e32 v22, 0, v22
	v_max_f32_e32 v23, 0, v23
	v_pk_mul_f32 v[24:25], v[22:23], s[2:3] op_sel_hi:[1,0]
	v_fmamk_f32 v19, v58, 0x3a800000, v2
	v_cvt_pk_f16_f32 v25, v24, v25
	v_max_f32_e32 v19, 0, v19
	v_cvt_f32_f16_e32 v34, v25
	v_cvt_f32_f16_sdwa v35, v25 dst_sel:DWORD dst_unused:UNUSED_PAD src0_sel:WORD_1
	v_fma_mixlo_f16 v20, v19, s2, 0
	v_mul_f32_e32 v21, 0x41800000, v19
	v_fma_mixlo_f16 v20, v19, s2, -v20 op_sel_hi:[0,0,1]
	v_fmamk_f32 v19, v59, 0x3a800000, v3
	v_max_f32_e32 v19, 0, v19
	v_mul_f32_e32 v36, 0x41800000, v19
	v_pk_fma_f32 v[22:23], v[22:23], s[2:3], v[34:35] op_sel_hi:[1,0,1] neg_lo:[0,0,1] neg_hi:[0,0,1]
	v_fma_mixlo_f16 v37, v19, s2, 0
	v_cvt_pk_f16_f32 v24, v21, v36
	v_cvt_pk_f16_f32 v21, v22, v23
	v_fmamk_f32 v22, v44, 0x3a800000, v4
	v_fmamk_f32 v23, v45, 0x3a800000, v5
	v_fma_mixhi_f16 v20, v19, s2, -v37 op_sel_hi:[0,0,1]
	v_max_f32_e32 v22, 0, v22
	v_max_f32_e32 v23, 0, v23
	ds_write2_b64 v73, v[24:25], v[20:21] offset0:8 offset1:10
	v_fmamk_f32 v19, v42, 0x3a800000, v2
	v_pk_mul_f32 v[24:25], v[22:23], s[2:3] op_sel_hi:[1,0]
	v_max_f32_e32 v19, 0, v19
	v_cvt_pk_f16_f32 v25, v24, v25
	v_fma_mixlo_f16 v20, v19, s2, 0
	v_cvt_f32_f16_e32 v34, v25
	v_cvt_f32_f16_sdwa v35, v25 dst_sel:DWORD dst_unused:UNUSED_PAD src0_sel:WORD_1
	v_mul_f32_e32 v21, 0x41800000, v19
	v_fma_mixlo_f16 v20, v19, s2, -v20 op_sel_hi:[0,0,1]
	v_fmamk_f32 v19, v43, 0x3a800000, v3
	v_max_f32_e32 v19, 0, v19
	v_fma_mixlo_f16 v37, v19, s2, 0
	v_mul_f32_e32 v36, 0x41800000, v19
	v_fma_mixhi_f16 v20, v19, s2, -v37 op_sel_hi:[0,0,1]
	v_pk_fma_f32 v[22:23], v[22:23], s[2:3], v[34:35] op_sel_hi:[1,0,1] neg_lo:[0,0,1] neg_hi:[0,0,1]
	v_fmamk_f32 v19, v26, 0x3a800000, v2
	v_cvt_pk_f16_f32 v24, v21, v36
	v_cvt_pk_f16_f32 v21, v22, v23
	v_max_f32_e32 v19, 0, v19
	ds_write2_b64 v72, v[24:25], v[20:21] offset0:72 offset1:74
	v_fma_mixlo_f16 v20, v19, s2, 0
	v_fmamk_f32 v22, v28, 0x3a800000, v4
	v_fmamk_f32 v23, v29, 0x3a800000, v5
	v_mul_f32_e32 v21, 0x41800000, v19
	v_fma_mixlo_f16 v20, v19, s2, -v20 op_sel_hi:[0,0,1]
	v_fmamk_f32 v19, v27, 0x3a800000, v3
	v_max_f32_e32 v22, 0, v22
	v_max_f32_e32 v23, 0, v23
	v_fmamk_f32 v2, v10, 0x3a800000, v2
	v_max_f32_e32 v19, 0, v19
	v_pk_mul_f32 v[24:25], v[22:23], s[2:3] op_sel_hi:[1,0]
	v_max_f32_e32 v2, 0, v2
	v_fmamk_f32 v4, v12, 0x3a800000, v4
	v_fmac_f32_e32 v5, 0x3a800000, v13
	v_cvt_pk_f16_f32 v25, v24, v25
	v_fma_mixlo_f16 v28, v19, s2, 0
	v_fma_mixlo_f16 v10, v2, s2, 0
	v_max_f32_e32 v4, 0, v4
	v_max_f32_e32 v5, 0, v5
	v_mul_f32_e32 v34, 0x41800000, v19
	v_cvt_f32_f16_e32 v26, v25
	v_cvt_f32_f16_sdwa v27, v25 dst_sel:DWORD dst_unused:UNUSED_PAD src0_sel:WORD_1
	v_fma_mixhi_f16 v20, v19, s2, -v28 op_sel_hi:[0,0,1]
	v_mul_f32_e32 v19, 0x41800000, v2
	v_fma_mixlo_f16 v2, v2, s2, -v10 op_sel_hi:[0,0,1]
	v_fmamk_f32 v3, v11, 0x3a800000, v3
	v_pk_mul_f32 v[10:11], v[4:5], s[2:3] op_sel_hi:[1,0]
	v_pk_fma_f32 v[22:23], v[22:23], s[2:3], v[26:27] op_sel_hi:[1,0,1] neg_lo:[0,0,1] neg_hi:[0,0,1]
	v_cvt_pk_f16_f32 v11, v10, v11
	v_cvt_f32_f16_e32 v12, v11
	v_cvt_f32_f16_sdwa v13, v11 dst_sel:DWORD dst_unused:UNUSED_PAD src0_sel:WORD_1
	v_cvt_pk_f16_f32 v24, v21, v34
	v_cvt_pk_f16_f32 v21, v22, v23
	v_max_f32_e32 v3, 0, v3
	ds_write2_b64 v71, v[24:25], v[20:21] offset0:136 offset1:138
	v_mul_f32_e32 v20, 0x41800000, v3
	v_fma_mixlo_f16 v21, v3, s2, 0
	v_pk_fma_f32 v[4:5], v[4:5], s[2:3], v[12:13] op_sel_hi:[1,0,1] neg_lo:[0,0,1] neg_hi:[0,0,1]
	v_cvt_pk_f16_f32 v10, v19, v20
	v_fma_mixhi_f16 v2, v3, s2, -v21 op_sel_hi:[0,0,1]
	v_cvt_pk_f16_f32 v3, v4, v5
	ds_write2_b64 v18, v[10:11], v[2:3] offset0:200 offset1:202
	s_waitcnt vmcnt(0)
	v_fmamk_f32 v2, v62, 0x3a800000, v6
	v_max_f32_e32 v2, 0, v2
	v_fma_mixlo_f16 v4, v2, s2, 0
	v_mul_f32_e32 v3, 0x41800000, v2
	v_fma_mixlo_f16 v2, v2, s2, -v4 op_sel_hi:[0,0,1]
	v_fmamk_f32 v4, v63, 0x3a800000, v7
	v_max_f32_e32 v19, 0, v4
	v_fmamk_f32 v4, v64, 0x3a800000, v8
	v_fmamk_f32 v5, v65, 0x3a800000, v9
	v_max_f32_e32 v4, 0, v4
	v_max_f32_e32 v5, 0, v5
	v_pk_mul_f32 v[10:11], v[4:5], s[2:3] op_sel_hi:[1,0]
	v_mul_f32_e32 v20, 0x41800000, v19
	v_cvt_pk_f16_f32 v11, v10, v11
	v_cvt_f32_f16_e32 v12, v11
	v_cvt_f32_f16_sdwa v13, v11 dst_sel:DWORD dst_unused:UNUSED_PAD src0_sel:WORD_1
	v_fma_mixlo_f16 v21, v19, s2, 0
	v_cvt_pk_f16_f32 v10, v3, v20
	v_fma_mixhi_f16 v2, v19, s2, -v21 op_sel_hi:[0,0,1]
	v_pk_fma_f32 v[4:5], v[4:5], s[2:3], v[12:13] op_sel_hi:[1,0,1] neg_lo:[0,0,1] neg_hi:[0,0,1]
	s_nop 0
	v_cvt_pk_f16_f32 v3, v4, v5
	ds_write2_b64 v73, v[10:11], v[2:3] offset0:12 offset1:14
	v_fmamk_f32 v2, v46, 0x3a800000, v6
	v_max_f32_e32 v2, 0, v2
	v_fma_mixlo_f16 v4, v2, s2, 0
	v_mul_f32_e32 v3, 0x41800000, v2
	v_fma_mixlo_f16 v2, v2, s2, -v4 op_sel_hi:[0,0,1]
	v_fmamk_f32 v4, v47, 0x3a800000, v7
	v_max_f32_e32 v19, 0, v4
	v_fmamk_f32 v4, v48, 0x3a800000, v8
	v_fmamk_f32 v5, v49, 0x3a800000, v9
	v_max_f32_e32 v4, 0, v4
	v_max_f32_e32 v5, 0, v5
	v_pk_mul_f32 v[10:11], v[4:5], s[2:3] op_sel_hi:[1,0]
	v_mul_f32_e32 v20, 0x41800000, v19
	v_cvt_pk_f16_f32 v11, v10, v11
	v_cvt_f32_f16_e32 v12, v11
	v_cvt_f32_f16_sdwa v13, v11 dst_sel:DWORD dst_unused:UNUSED_PAD src0_sel:WORD_1
	v_fma_mixlo_f16 v21, v19, s2, 0
	v_cvt_pk_f16_f32 v10, v3, v20
	v_fma_mixhi_f16 v2, v19, s2, -v21 op_sel_hi:[0,0,1]
	v_pk_fma_f32 v[4:5], v[4:5], s[2:3], v[12:13] op_sel_hi:[1,0,1] neg_lo:[0,0,1] neg_hi:[0,0,1]
	s_nop 0
	v_cvt_pk_f16_f32 v3, v4, v5
	ds_write2_b64 v72, v[10:11], v[2:3] offset0:76 offset1:78
	v_fmamk_f32 v2, v30, 0x3a800000, v6
	v_max_f32_e32 v2, 0, v2
	v_fma_mixlo_f16 v4, v2, s2, 0
	v_mul_f32_e32 v3, 0x41800000, v2
	v_fma_mixlo_f16 v2, v2, s2, -v4 op_sel_hi:[0,0,1]
	v_fmamk_f32 v4, v31, 0x3a800000, v7
	v_max_f32_e32 v19, 0, v4
	v_fmamk_f32 v4, v32, 0x3a800000, v8
	v_fmamk_f32 v5, v33, 0x3a800000, v9
	v_max_f32_e32 v4, 0, v4
	v_max_f32_e32 v5, 0, v5
	v_pk_mul_f32 v[10:11], v[4:5], s[2:3] op_sel_hi:[1,0]
	v_mul_f32_e32 v20, 0x41800000, v19
	v_cvt_pk_f16_f32 v11, v10, v11
	v_cvt_f32_f16_e32 v12, v11
	v_cvt_f32_f16_sdwa v13, v11 dst_sel:DWORD dst_unused:UNUSED_PAD src0_sel:WORD_1
	v_fma_mixlo_f16 v21, v19, s2, 0
	v_cvt_pk_f16_f32 v10, v3, v20
	v_fma_mixhi_f16 v2, v19, s2, -v21 op_sel_hi:[0,0,1]
	v_pk_fma_f32 v[4:5], v[4:5], s[2:3], v[12:13] op_sel_hi:[1,0,1] neg_lo:[0,0,1] neg_hi:[0,0,1]
	v_fmac_f32_e32 v9, 0x3a800000, v17
	v_cvt_pk_f16_f32 v3, v4, v5
	ds_write2_b64 v71, v[10:11], v[2:3] offset0:140 offset1:142
	v_fmamk_f32 v2, v14, 0x3a800000, v6
	v_max_f32_e32 v2, 0, v2
	v_fma_mixlo_f16 v4, v2, s2, 0
	v_mul_f32_e32 v3, 0x41800000, v2
	v_fma_mixlo_f16 v2, v2, s2, -v4 op_sel_hi:[0,0,1]
	v_fmamk_f32 v4, v15, 0x3a800000, v7
	v_max_f32_e32 v10, 0, v4
	v_fmamk_f32 v4, v16, 0x3a800000, v8
	v_max_f32_e32 v4, 0, v4
	v_max_f32_e32 v5, 0, v9
	v_pk_mul_f32 v[6:7], v[4:5], s[2:3] op_sel_hi:[1,0]
	v_fma_mixlo_f16 v12, v10, s2, 0
	v_cvt_pk_f16_f32 v7, v6, v7
	v_cvt_f32_f16_e32 v8, v7
	v_cvt_f32_f16_sdwa v9, v7 dst_sel:DWORD dst_unused:UNUSED_PAD src0_sel:WORD_1
	v_mul_f32_e32 v11, 0x41800000, v10
	v_fma_mixhi_f16 v2, v10, s2, -v12 op_sel_hi:[0,0,1]
	v_cvt_pk_f16_f32 v6, v3, v11
	v_pk_fma_f32 v[4:5], v[4:5], s[2:3], v[8:9] op_sel_hi:[1,0,1] neg_lo:[0,0,1] neg_hi:[0,0,1]
	s_movk_i32 s2, 0x80
	v_cvt_pk_f16_f32 v3, v4, v5
	v_cmp_gt_u32_e32 vcc, s2, v0
	ds_write2_b64 v18, v[6:7], v[2:3] offset0:204 offset1:206
	s_waitcnt lgkmcnt(0)
	s_barrier
	s_and_saveexec_b64 s[2:3], vcc
	s_cbranch_execz .LBB6_74
	global_load_dwordx4 v[112:115], v80, s[12:13]
	global_load_dwordx4 v[116:119], v80, s[12:13] offset:32
	global_load_dwordx4 v[120:123], v80, s[12:13] offset:64
	global_load_dwordx4 v[124:127], v80, s[12:13] offset:96
	v_mov_b32_e32 v3, 0
	v_lshlrev_b32_e32 v2, 4, v1
	v_lshl_add_u64 v[0:1], s[0:1], 0, v[2:3]
	v_lshlrev_b32_e32 v2, 11, v70
	v_lshl_add_u64 v[72:73], v[0:1], 0, v[2:3]
	v_add_co_u32_e32 v4, vcc, 0x1000, v72
	s_nop 1
	v_addc_co_u32_e32 v5, vcc, 0, v73, vcc
	global_load_dwordx4 v[0:3], v[72:73], off
	global_load_dwordx4 v[64:67], v[4:5], off
	v_mul_u32_u24_e32 v4, 0x210, v180
	v_add_u32_e32 v75, v4, v181
	ds_read_b128 v[4:7], v75
	ds_read_b128 v[68:71], v75 offset:64
	ds_read_b128 v[8:11], v75 offset:16896
	ds_read_b128 v[76:79], v75 offset:16960
	ds_read_b128 v[12:15], v75 offset:33792
	ds_read_b128 v[82:85], v75 offset:33856
	ds_read_b128 v[86:89], v75 offset:50688
	ds_read_b128 v[90:93], v75 offset:50752
	s_waitcnt vmcnt(1) lgkmcnt(7)
	v_mfma_f32_32x32x16_f16 v[48:63], v[0:3], v[4:7], 0
	s_waitcnt lgkmcnt(5)
	v_mfma_f32_32x32x16_f16 v[32:47], v[0:3], v[8:11], 0
	s_waitcnt lgkmcnt(3)
	v_mfma_f32_32x32x16_f16 v[16:31], v[0:3], v[12:15], 0
	s_waitcnt lgkmcnt(1)
	v_mfma_f32_32x32x16_f16 v[0:15], v[0:3], v[86:89], 0
	s_movk_i32 s0, 0x3000
	v_add_co_u32_e32 v110, vcc, s0, v72
	s_nop 1
	v_addc_co_u32_e32 v111, vcc, 0, v73, vcc
	global_load_dwordx4 v[86:89], v[110:111], off offset:-4096
	ds_read_b128 v[94:97], v75 offset:128
	ds_read_b128 v[98:101], v75 offset:17024
	ds_read_b128 v[102:105], v75 offset:33920
	ds_read_b128 v[106:109], v75 offset:50816
	s_waitcnt vmcnt(1)
	v_mfma_f32_32x32x16_f16 v[48:63], v[64:67], v[68:71], v[48:63]
	v_mfma_f32_32x32x16_f16 v[32:47], v[64:67], v[76:79], v[32:47]
	v_mfma_f32_32x32x16_f16 v[16:31], v[64:67], v[82:85], v[16:31]
	s_waitcnt lgkmcnt(4)
	v_mfma_f32_32x32x16_f16 v[0:15], v[64:67], v[90:93], v[0:15]
	global_load_dwordx4 v[64:67], v[110:111], off
	ds_read_b128 v[68:71], v75 offset:192
	ds_read_b128 v[76:79], v75 offset:17088
	ds_read_b128 v[82:85], v75 offset:33984
	ds_read_b128 v[90:93], v75 offset:50880
	s_waitcnt vmcnt(1) lgkmcnt(7)
	v_mfma_f32_32x32x16_f16 v[48:63], v[86:89], v[94:97], v[48:63]
	s_waitcnt lgkmcnt(6)
	v_mfma_f32_32x32x16_f16 v[32:47], v[86:89], v[98:101], v[32:47]
	s_waitcnt lgkmcnt(5)
	v_mfma_f32_32x32x16_f16 v[16:31], v[86:89], v[102:105], v[16:31]
	s_waitcnt lgkmcnt(4)
	v_mfma_f32_32x32x16_f16 v[0:15], v[86:89], v[106:109], v[0:15]
	s_movk_i32 s0, 0x5000
	v_add_co_u32_e32 v110, vcc, s0, v72
	s_nop 1
	v_addc_co_u32_e32 v111, vcc, 0, v73, vcc
	global_load_dwordx4 v[86:89], v[110:111], off offset:-4096
	ds_read_b128 v[94:97], v75 offset:256
	ds_read_b128 v[98:101], v75 offset:17152
	ds_read_b128 v[102:105], v75 offset:34048
	ds_read_b128 v[106:109], v75 offset:50944
	s_waitcnt vmcnt(1) lgkmcnt(7)
	v_mfma_f32_32x32x16_f16 v[48:63], v[64:67], v[68:71], v[48:63]
	s_waitcnt lgkmcnt(6)
	v_mfma_f32_32x32x16_f16 v[32:47], v[64:67], v[76:79], v[32:47]
	s_waitcnt lgkmcnt(5)
	v_mfma_f32_32x32x16_f16 v[16:31], v[64:67], v[82:85], v[16:31]
	s_waitcnt lgkmcnt(4)
	v_mfma_f32_32x32x16_f16 v[0:15], v[64:67], v[90:93], v[0:15]
	global_load_dwordx4 v[64:67], v[110:111], off
	ds_read_b128 v[68:71], v75 offset:320
	ds_read_b128 v[76:79], v75 offset:17216
	ds_read_b128 v[82:85], v75 offset:34112
	ds_read_b128 v[90:93], v75 offset:51008
	s_waitcnt vmcnt(1) lgkmcnt(7)
	v_mfma_f32_32x32x16_f16 v[48:63], v[86:89], v[94:97], v[48:63]
	s_waitcnt lgkmcnt(6)
	v_mfma_f32_32x32x16_f16 v[32:47], v[86:89], v[98:101], v[32:47]
	s_waitcnt lgkmcnt(5)
	v_mfma_f32_32x32x16_f16 v[16:31], v[86:89], v[102:105], v[16:31]
	s_waitcnt lgkmcnt(4)
	v_mfma_f32_32x32x16_f16 v[0:15], v[86:89], v[106:109], v[0:15]
	s_movk_i32 s0, 0x7000
	v_add_co_u32_e32 v72, vcc, s0, v72
	s_nop 1
	v_addc_co_u32_e32 v73, vcc, 0, v73, vcc
	global_load_dwordx4 v[86:89], v[72:73], off offset:-4096
	ds_read_b128 v[94:97], v75 offset:384
	ds_read_b128 v[98:101], v75 offset:17280
	ds_read_b128 v[102:105], v75 offset:34176
	ds_read_b128 v[106:109], v75 offset:51072
	s_waitcnt vmcnt(1) lgkmcnt(7)
	v_mfma_f32_32x32x16_f16 v[48:63], v[64:67], v[68:71], v[48:63]
	s_waitcnt lgkmcnt(6)
	v_mfma_f32_32x32x16_f16 v[32:47], v[64:67], v[76:79], v[32:47]
	s_waitcnt lgkmcnt(5)
	v_mfma_f32_32x32x16_f16 v[16:31], v[64:67], v[82:85], v[16:31]
	s_waitcnt lgkmcnt(4)
	v_mfma_f32_32x32x16_f16 v[0:15], v[64:67], v[90:93], v[0:15]
	global_load_dwordx4 v[64:67], v[72:73], off
	ds_read_b128 v[68:71], v75 offset:448
	ds_read_b128 v[76:79], v75 offset:17344
	ds_read_b128 v[82:85], v75 offset:34240
	ds_read_b128 v[90:93], v75 offset:51136
	s_waitcnt vmcnt(1) lgkmcnt(7)
	v_mfma_f32_32x32x16_f16 v[48:63], v[86:89], v[94:97], v[48:63]
	s_waitcnt lgkmcnt(6)
	v_mfma_f32_32x32x16_f16 v[32:47], v[86:89], v[98:101], v[32:47]
	s_waitcnt lgkmcnt(5)
	v_mfma_f32_32x32x16_f16 v[16:31], v[86:89], v[102:105], v[16:31]
	s_waitcnt lgkmcnt(4)
	v_mfma_f32_32x32x16_f16 v[0:15], v[86:89], v[106:109], v[0:15]
	s_waitcnt vmcnt(0) lgkmcnt(3)
	v_mfma_f32_32x32x16_f16 v[48:63], v[64:67], v[68:71], v[48:63]
	s_waitcnt lgkmcnt(2)
	v_mfma_f32_32x32x16_f16 v[32:47], v[64:67], v[76:79], v[32:47]
	s_waitcnt lgkmcnt(1)
	v_mfma_f32_32x32x16_f16 v[16:31], v[64:67], v[82:85], v[16:31]
	s_waitcnt lgkmcnt(0)
	v_mfma_f32_32x32x16_f16 v[0:15], v[64:67], v[90:93], v[0:15]
	v_readfirstlane_b32 s24, v74
	v_and_b32_e32 v86, 4, v74
	v_lshlrev_b32_e32 v86, 14, v86
	v_lshl_add_u32 v86, v180, 2, v86
	s_lshl_b32 s25, s4, 20
	s_nop 3
	s_lshr_b32 s24, s24, 5
	s_lshl_b32 s24, s24, 19
	s_add_u32 s25, s25, s24
	s_lshl_b32 s24, s20, 8
	s_add_u32 s25, s25, s24
	s_lshl_b32 s24, s5, 2
	s_add_u32 s25, s25, s24
	s_add_u32 s22, s14, s25
	s_addc_u32 s23, s15, 0
	s_waitcnt vmcnt(0)
	v_fmamk_f32 v48, v48, 0x3a800000, v112
	v_fmamk_f32 v32, v32, 0x3a800000, v112
	v_fmamk_f32 v16, v16, 0x3a800000, v112
	v_fmamk_f32 v0, v0, 0x3a800000, v112
	global_store_dword v86, v48, s[22:23]
	global_store_dword v86, v32, s[22:23] offset:256
	global_store_dword v86, v16, s[22:23] offset:512
	global_store_dword v86, v0, s[22:23] offset:768
	s_add_u32 s22, s22, 0x4000
	s_addc_u32 s23, s23, 0
	v_fmamk_f32 v49, v49, 0x3a800000, v113
	v_fmamk_f32 v33, v33, 0x3a800000, v113
	v_fmamk_f32 v17, v17, 0x3a800000, v113
	v_fmamk_f32 v1, v1, 0x3a800000, v113
	global_store_dword v86, v49, s[22:23]
	global_store_dword v86, v33, s[22:23] offset:256
	global_store_dword v86, v17, s[22:23] offset:512
	global_store_dword v86, v1, s[22:23] offset:768
	s_add_u32 s22, s22, 0x4000
	s_addc_u32 s23, s23, 0
	v_fmamk_f32 v50, v50, 0x3a800000, v114
	v_fmamk_f32 v34, v34, 0x3a800000, v114
	v_fmamk_f32 v18, v18, 0x3a800000, v114
	v_fmamk_f32 v2, v2, 0x3a800000, v114
	global_store_dword v86, v50, s[22:23]
	global_store_dword v86, v34, s[22:23] offset:256
	global_store_dword v86, v18, s[22:23] offset:512
	global_store_dword v86, v2, s[22:23] offset:768
	s_add_u32 s22, s22, 0x4000
	s_addc_u32 s23, s23, 0
	v_fmamk_f32 v51, v51, 0x3a800000, v115
	v_fmamk_f32 v35, v35, 0x3a800000, v115
	v_fmamk_f32 v19, v19, 0x3a800000, v115
	v_fmamk_f32 v3, v3, 0x3a800000, v115
	global_store_dword v86, v51, s[22:23]
	global_store_dword v86, v35, s[22:23] offset:256
	global_store_dword v86, v19, s[22:23] offset:512
	global_store_dword v86, v3, s[22:23] offset:768
	s_add_u32 s22, s22, 0x14000
	s_addc_u32 s23, s23, 0
	v_fmamk_f32 v52, v52, 0x3a800000, v116
	v_fmamk_f32 v36, v36, 0x3a800000, v116
	v_fmamk_f32 v20, v20, 0x3a800000, v116
	v_fmamk_f32 v4, v4, 0x3a800000, v116
	global_store_dword v86, v52, s[22:23]
	global_store_dword v86, v36, s[22:23] offset:256
	global_store_dword v86, v20, s[22:23] offset:512
	global_store_dword v86, v4, s[22:23] offset:768
	s_add_u32 s22, s22, 0x4000
	s_addc_u32 s23, s23, 0
	v_fmamk_f32 v53, v53, 0x3a800000, v117
	v_fmamk_f32 v37, v37, 0x3a800000, v117
	v_fmamk_f32 v21, v21, 0x3a800000, v117
	v_fmamk_f32 v5, v5, 0x3a800000, v117
	global_store_dword v86, v53, s[22:23]
	global_store_dword v86, v37, s[22:23] offset:256
	global_store_dword v86, v21, s[22:23] offset:512
	global_store_dword v86, v5, s[22:23] offset:768
	s_add_u32 s22, s22, 0x4000
	s_addc_u32 s23, s23, 0
	v_fmamk_f32 v54, v54, 0x3a800000, v118
	v_fmamk_f32 v38, v38, 0x3a800000, v118
	v_fmamk_f32 v22, v22, 0x3a800000, v118
	v_fmamk_f32 v6, v6, 0x3a800000, v118
	global_store_dword v86, v54, s[22:23]
	global_store_dword v86, v38, s[22:23] offset:256
	global_store_dword v86, v22, s[22:23] offset:512
	global_store_dword v86, v6, s[22:23] offset:768
	s_add_u32 s22, s22, 0x4000
	s_addc_u32 s23, s23, 0
	v_fmamk_f32 v55, v55, 0x3a800000, v119
	v_fmamk_f32 v39, v39, 0x3a800000, v119
	v_fmamk_f32 v23, v23, 0x3a800000, v119
	v_fmamk_f32 v7, v7, 0x3a800000, v119
	global_store_dword v86, v55, s[22:23]
	global_store_dword v86, v39, s[22:23] offset:256
	global_store_dword v86, v23, s[22:23] offset:512
	global_store_dword v86, v7, s[22:23] offset:768
	s_add_u32 s22, s22, 0x14000
	s_addc_u32 s23, s23, 0
	v_fmamk_f32 v56, v56, 0x3a800000, v120
	v_fmamk_f32 v40, v40, 0x3a800000, v120
	v_fmamk_f32 v24, v24, 0x3a800000, v120
	v_fmamk_f32 v8, v8, 0x3a800000, v120
	global_store_dword v86, v56, s[22:23]
	global_store_dword v86, v40, s[22:23] offset:256
	global_store_dword v86, v24, s[22:23] offset:512
	global_store_dword v86, v8, s[22:23] offset:768
	s_add_u32 s22, s22, 0x4000
	s_addc_u32 s23, s23, 0
	v_fmamk_f32 v57, v57, 0x3a800000, v121
	v_fmamk_f32 v41, v41, 0x3a800000, v121
	v_fmamk_f32 v25, v25, 0x3a800000, v121
	v_fmamk_f32 v9, v9, 0x3a800000, v121
	global_store_dword v86, v57, s[22:23]
	global_store_dword v86, v41, s[22:23] offset:256
	global_store_dword v86, v25, s[22:23] offset:512
	global_store_dword v86, v9, s[22:23] offset:768
	s_add_u32 s22, s22, 0x4000
	s_addc_u32 s23, s23, 0
	v_fmamk_f32 v58, v58, 0x3a800000, v122
	v_fmamk_f32 v42, v42, 0x3a800000, v122
	v_fmamk_f32 v26, v26, 0x3a800000, v122
	v_fmamk_f32 v10, v10, 0x3a800000, v122
	global_store_dword v86, v58, s[22:23]
	global_store_dword v86, v42, s[22:23] offset:256
	global_store_dword v86, v26, s[22:23] offset:512
	global_store_dword v86, v10, s[22:23] offset:768
	s_add_u32 s22, s22, 0x4000
	s_addc_u32 s23, s23, 0
	v_fmamk_f32 v59, v59, 0x3a800000, v123
	v_fmamk_f32 v43, v43, 0x3a800000, v123
	v_fmamk_f32 v27, v27, 0x3a800000, v123
	v_fmamk_f32 v11, v11, 0x3a800000, v123
	global_store_dword v86, v59, s[22:23]
	global_store_dword v86, v43, s[22:23] offset:256
	global_store_dword v86, v27, s[22:23] offset:512
	global_store_dword v86, v11, s[22:23] offset:768
	s_add_u32 s22, s22, 0x14000
	s_addc_u32 s23, s23, 0
	v_fmamk_f32 v60, v60, 0x3a800000, v124
	v_fmamk_f32 v44, v44, 0x3a800000, v124
	v_fmamk_f32 v28, v28, 0x3a800000, v124
	v_fmamk_f32 v12, v12, 0x3a800000, v124
	global_store_dword v86, v60, s[22:23]
	global_store_dword v86, v44, s[22:23] offset:256
	global_store_dword v86, v28, s[22:23] offset:512
	global_store_dword v86, v12, s[22:23] offset:768
	s_add_u32 s22, s22, 0x4000
	s_addc_u32 s23, s23, 0
	v_fmamk_f32 v61, v61, 0x3a800000, v125
	v_fmamk_f32 v45, v45, 0x3a800000, v125
	v_fmamk_f32 v29, v29, 0x3a800000, v125
	v_fmamk_f32 v13, v13, 0x3a800000, v125
	global_store_dword v86, v61, s[22:23]
	global_store_dword v86, v45, s[22:23] offset:256
	global_store_dword v86, v29, s[22:23] offset:512
	global_store_dword v86, v13, s[22:23] offset:768
	s_add_u32 s22, s22, 0x4000
	s_addc_u32 s23, s23, 0
	v_fmamk_f32 v62, v62, 0x3a800000, v126
	v_fmamk_f32 v46, v46, 0x3a800000, v126
	v_fmamk_f32 v30, v30, 0x3a800000, v126
	v_fmamk_f32 v14, v14, 0x3a800000, v126
	global_store_dword v86, v62, s[22:23]
	global_store_dword v86, v46, s[22:23] offset:256
	global_store_dword v86, v30, s[22:23] offset:512
	global_store_dword v86, v14, s[22:23] offset:768
	s_add_u32 s22, s22, 0x4000
	s_addc_u32 s23, s23, 0
	v_fmamk_f32 v63, v63, 0x3a800000, v127
	v_fmamk_f32 v47, v47, 0x3a800000, v127
	v_fmamk_f32 v31, v31, 0x3a800000, v127
	v_fmamk_f32 v15, v15, 0x3a800000, v127
	global_store_dword v86, v63, s[22:23]
	global_store_dword v86, v47, s[22:23] offset:256
	global_store_dword v86, v31, s[22:23] offset:512
	global_store_dword v86, v15, s[22:23] offset:768
